# removed LDS-DMA hazard pads that guard nothing (SALU-computed bases) in both attention loops; indexer pass-1 bin sum + address in two instructions
# speedup vs baseline: 1.0217x; 1.0050x over previous
; #define SB_STAGE(j_, so_) do { const size_t ro_ = (size_t)(j_) * 64 * D; glds16_s(Kwa + ro_, kvoff, kda + (so_)); glds16_s(Kwb + ro_, kvoff, kdb + (so_)); glds16_s(Vwa + ro_, vvoff, vda + (so_)); glds16_s(Vwb + ro_, vvoff, vdb + (so_)); } while (0)
; __device__ __forceinline__ void sb_block_unit(bf16x8 (&qr)[4], int b, int hp  , int u  , int nb, int nhp, int nu, const bf16_t* Q, const bf16_t* K, const bf16_t* V, bf16_t* O, LAS char* L, int wid, int lane) {
;     ...
;     f32x16 o[2]; o[0] = f32x16{}; o[1] = f32x16{};
;     float carry = 1.f; bool gone = false;
;     asm volatile("s_waitcnt vmcnt(0) lgkmcnt(0)\n\ts_barrier" ::: "memory");
;     int sc = 0, sn = SL_SLOT, sn2 = 2 * SL_SLOT;
;     for (int j = jtop; j >= 0; --j) {
;         if (j >= 2) SB_STAGE(j - 2, (unsigned)sn2);
.LBB0_356:
	s_cmp_lt_u32 s33, 2
	s_cselect_b64 s[92:93], -1, 0
	s_mov_b32 s1, s88
	s_and_b64 vcc, exec, s[92:93]
	s_cbranch_vccnz .LBB0_358
	v_readlane_b32 s86, v254, 55
	v_readlane_b32 s87, v254, 56
	s_mov_b32 s89, s87
	s_add_i32 s88, s33, -2
	v_writelane_b32 v254, s86, 55
	s_lshl_b64 s[88:89], s[88:89], 17
	s_add_u32 s94, s83, s88
	v_writelane_b32 v254, s87, 56
	s_addc_u32 s95, s80, s89
	v_readlane_b32 s86, v254, 5
	s_add_i32 s86, s84, s86
	s_mov_b32 s87, m0
	s_mov_b32 m0, s86
	s_nop 0
	global_load_lds_dwordx4 v142, s[94:95]
	s_mov_b32 m0, s87
	s_add_u32 s94, s3, s88
	v_readlane_b32 s86, v254, 7
	s_addc_u32 s95, s78, s89
	s_add_i32 s86, s84, s86
	s_mov_b32 s87, m0
	s_mov_b32 m0, s86
	s_nop 0
	global_load_lds_dwordx4 v142, s[94:95]
	s_mov_b32 m0, s87
	s_add_u32 s94, s2, s88
	v_readlane_b32 s86, v254, 9
	s_addc_u32 s95, s6, s89
	s_add_i32 s86, s84, s86
	s_mov_b32 s87, m0
	s_mov_b32 m0, s86
	s_nop 0
	global_load_lds_dwordx4 v145, s[94:95]
	s_mov_b32 m0, s87
	s_add_u32 s88, s81, s88
	v_readlane_b32 s86, v254, 11
	s_addc_u32 s89, s0, s89
	s_add_i32 s86, s84, s86
	s_mov_b32 s87, m0
	s_mov_b32 m0, s86
	s_nop 0
	global_load_lds_dwordx4 v145, s[88:89]
	s_mov_b32 m0, s87

; #define LAS __attribute__((address_space(3)))
; template <int PASS, bool DIAG> __device__ __forceinline__ void idx_half(unsigned& bits, unsigned& ebits, const f32x16& sc, int sbase, int tq, int r32, int hi, unsigned khi, unsigned klo, bool cand, LAS unsigned char* L) {
;     ...
;         LAS unsigned* H = (LAS unsigned*)(L + IL_HIST) + r32 * HSTR + 160;
; #pragma unroll
;         for (int r = 0; r < 16; ++r) { int b = ibin_u_m160(__float_as_uint(sc[r] + 0.0f)); asm("" : "+v"(b));
; template <int PASS> __device__ __forceinline__ void idx_pass(const bf16_t* KIb, const bf16x8 (&qf)[16], const f32x4& w, int jd, int tq, int wid, int r32, int hi, unsigned khi, unsigned klo, bool cand, LAS unsigned char* L) {
;     bf16x8 kA[4], kB[4];
;     int j = wid;
;     if (j <= jd) idx_loadk(kA, KIb + (size_t)(j * 64) * 64, r32, hi);
;     for (; j <= jd; j += 8) {
.LBB0_710:
	v_lshlrev_b32_e32 v0, 7, v222
	v_lshl_add_u64 v[2:3], s[38:39], 0, v[0:1]
	v_lshlrev_b32_e32 v0, 4, v223
	v_lshl_add_u64 v[50:51], v[2:3], 0, v[0:1]
	s_movk_i32 s0, 0x504
	v_lshlrev_b32_e32 v2, 2, v223
	v_add_u32_e32 v3, s62, v222
	v_mad_u32_u24 v0, v222, s0, 0
	v_add_u32_e32 v234, 0xfffff160, v0
	s_lshl_b32 s0, s64, 6
	v_sub_u32_e32 v2, v3, v2
	s_add_i32 s10, s0, 0x200
	s_add_i32 s20, s64, 8
	v_subrev_u32_e32 v52, s0, v2
	s_sub_i32 s21, 0, s65
	s_branch .LBB0_712

; __device__ __forceinline__ float relu_i(float p) { const int i = __float_as_int(p); return __int_as_float(i > 0 ? i : 0); }
; __device__ __forceinline__ void idx_scores_k(f32x16& sc, const bf16x8 (&kf)[4], const bf16x8 (&qf)[16], const f32x4& w) {
;     f32x16 p0 = f32x16{}, p1 = f32x16{};
; #pragma unroll
;     for (int d0 = 0; d0 < 4; ++d0) p0 = __builtin_amdgcn_mfma_f32_32x32x16_bf16(kf[d0], qf[d0], p0, 0, 0, 0);
; #pragma unroll
;     for (int d0 = 0; d0 < 4; ++d0) p1 = __builtin_amdgcn_mfma_f32_32x32x16_bf16(kf[d0], qf[4 + d0], p1, 0, 0, 0);
; #pragma unroll
;     for (int r = 0; r < 16; ++r) sc[r] = w[0] * relu_i(p0[r]);
;     p0 = f32x16{};
; #pragma unroll
;     for (int d0 = 0; d0 < 4; ++d0) p0 = __builtin_amdgcn_mfma_f32_32x32x16_bf16(kf[d0], qf[8 + d0], p0, 0, 0, 0);
; #pragma unroll
;     for (int r = 0; r < 16; ++r) sc[r] = fmaf(w[1], relu_i(p1[r]), sc[r]);
;     p1 = f32x16{};
; #pragma unroll
;     for (int d0 = 0; d0 < 4; ++d0) p1 = __builtin_amdgcn_mfma_f32_32x32x16_bf16(kf[d0], qf[12 + d0], p1, 0, 0, 0);
; #pragma unroll
;     for (int r = 0; r < 16; ++r) sc[r] = fmaf(w[2], relu_i(p0[r]), sc[r]);
; #pragma unroll
;     for (int r = 0; r < 16; ++r) sc[r] = fmaf(w[3], relu_i(p1[r]), sc[r]);
; }
; template <int PASS> __device__ __forceinline__ void idx_pass(const bf16_t* KIb, const bf16x8 (&qf)[16], const f32x4& w, int jd, int tq, int wid, int r32, int hi, unsigned khi, unsigned klo, bool cand, LAS unsigned char* L) {
;     ...
;     for (; j <= jd; j += 8) {
;         const bool diag = (j == jd);
;         idx_loadk(kB, KIb + (size_t)(j * 64 + 32) * 64, r32, hi);
;         f32x16 sc; idx_scores_k(sc, kA, qf, w);
.LBB0_712:
	s_add_i32 s0, s21, s20
	s_cmp_lg_u32 s0, 8
	s_cselect_b64 s[14:15], -1, 0
	s_add_i32 s0, s10, 0xfffffe20
	s_ashr_i32 s1, s0, 31
	s_lshl_b64 s[0:1], s[0:1], 7
	v_lshl_add_u64 v[2:3], v[50:51], 0, s[0:1]
	global_load_dwordx4 v[46:49], v[2:3], off
	global_load_dwordx4 v[42:45], v[2:3], off offset:32
	global_load_dwordx4 v[38:41], v[2:3], off offset:64
	global_load_dwordx4 v[34:37], v[2:3], off offset:96
	s_and_b64 vcc, exec, s[14:15]
	s_waitcnt vmcnt(7) lgkmcnt(14)
	v_mfma_f32_32x32x16_bf16 v[2:17], v[18:21], v[70:73], 0
	s_waitcnt vmcnt(6)
	v_mfma_f32_32x32x16_bf16 v[2:17], v[22:25], v[74:77], v[2:17]
	s_waitcnt vmcnt(5) lgkmcnt(13)
	v_mfma_f32_32x32x16_bf16 v[2:17], v[26:29], v[78:81], v[2:17]
	s_waitcnt vmcnt(4) lgkmcnt(12)
	v_mfma_f32_32x32x16_bf16 v[2:17], v[30:33], v[82:85], v[2:17]
	s_waitcnt lgkmcnt(11)
	v_mfma_f32_32x32x16_bf16 v[180:195], v[18:21], v[86:89], 0
	s_waitcnt lgkmcnt(10)
	v_mfma_f32_32x32x16_bf16 v[180:195], v[22:25], v[90:93], v[180:195]
	s_waitcnt lgkmcnt(9)
	v_mfma_f32_32x32x16_bf16 v[180:195], v[26:29], v[94:97], v[180:195]
	s_waitcnt lgkmcnt(8)
	v_mfma_f32_32x32x16_bf16 v[180:195], v[30:33], v[98:101], v[180:195]
	s_nop 3
	v_max_i32_e32 v200, 0, v2
	v_fma_f32 v136, v66, v200, 0
	v_max_i32_e32 v200, 0, v3
	v_fma_f32 v135, v66, v200, 0
	v_max_i32_e32 v200, 0, v4
	v_fma_f32 v134, v66, v200, 0
	v_max_i32_e32 v200, 0, v5
	v_fma_f32 v65, v66, v200, 0
	v_max_i32_e32 v200, 0, v6
	v_fma_f32 v64, v66, v200, 0
	v_max_i32_e32 v200, 0, v7
	v_fma_f32 v63, v66, v200, 0
	v_max_i32_e32 v200, 0, v8
	v_fma_f32 v62, v66, v200, 0
	v_max_i32_e32 v200, 0, v9
	v_fma_f32 v61, v66, v200, 0
	v_max_i32_e32 v200, 0, v10
	v_fma_f32 v60, v66, v200, 0
	v_max_i32_e32 v200, 0, v11
	v_fma_f32 v59, v66, v200, 0
	v_max_i32_e32 v200, 0, v12
	v_fma_f32 v58, v66, v200, 0
	v_max_i32_e32 v200, 0, v13
	v_fma_f32 v57, v66, v200, 0
	v_max_i32_e32 v200, 0, v14
	v_fma_f32 v56, v66, v200, 0
	v_max_i32_e32 v200, 0, v15
	v_fma_f32 v55, v66, v200, 0
	v_max_i32_e32 v200, 0, v16
	v_fma_f32 v54, v66, v200, 0
	v_max_i32_e32 v200, 0, v17
	v_fma_f32 v53, v66, v200, 0
	s_waitcnt lgkmcnt(7)
	v_mfma_f32_32x32x16_bf16 v[2:17], v[18:21], v[102:105], 0
	s_waitcnt lgkmcnt(6)
	v_mfma_f32_32x32x16_bf16 v[2:17], v[22:25], v[106:109], v[2:17]
	s_waitcnt lgkmcnt(5)
	v_mfma_f32_32x32x16_bf16 v[2:17], v[26:29], v[110:113], v[2:17]
	s_waitcnt lgkmcnt(4)
	v_mfma_f32_32x32x16_bf16 v[2:17], v[30:33], v[114:117], v[2:17]
	v_max_i32_e32 v200, 0, v180
	v_fmac_f32_e32 v136, v67, v200
	v_max_i32_e32 v200, 0, v181
	v_fmac_f32_e32 v135, v67, v200
	v_max_i32_e32 v200, 0, v182
	v_fmac_f32_e32 v134, v67, v200
	v_max_i32_e32 v200, 0, v183
	v_fmac_f32_e32 v65, v67, v200
	v_max_i32_e32 v200, 0, v184
	v_fmac_f32_e32 v64, v67, v200
	v_max_i32_e32 v200, 0, v185
	v_fmac_f32_e32 v63, v67, v200
	v_max_i32_e32 v200, 0, v186
	v_fmac_f32_e32 v62, v67, v200
	v_max_i32_e32 v200, 0, v187
	v_fmac_f32_e32 v61, v67, v200
	v_max_i32_e32 v200, 0, v188
	v_fmac_f32_e32 v60, v67, v200
	v_max_i32_e32 v200, 0, v189
	v_fmac_f32_e32 v59, v67, v200
	v_max_i32_e32 v200, 0, v190
	v_fmac_f32_e32 v58, v67, v200
	v_max_i32_e32 v200, 0, v191
	v_fmac_f32_e32 v57, v67, v200
	v_max_i32_e32 v200, 0, v192
	v_fmac_f32_e32 v56, v67, v200
	v_max_i32_e32 v200, 0, v193
	v_fmac_f32_e32 v55, v67, v200
	v_max_i32_e32 v200, 0, v194
	v_fmac_f32_e32 v54, v67, v200
	v_max_i32_e32 v200, 0, v195
	v_fmac_f32_e32 v53, v67, v200
	s_waitcnt lgkmcnt(3)
	v_mfma_f32_32x32x16_bf16 v[180:195], v[18:21], v[118:121], 0
	s_waitcnt lgkmcnt(2)
	v_mfma_f32_32x32x16_bf16 v[180:195], v[22:25], v[122:125], v[180:195]
	s_waitcnt lgkmcnt(1)
	v_mfma_f32_32x32x16_bf16 v[180:195], v[26:29], v[126:129], v[180:195]
	s_waitcnt lgkmcnt(0)
	v_mfma_f32_32x32x16_bf16 v[180:195], v[30:33], v[130:133], v[180:195]
	v_max_i32_e32 v200, 0, v2
	v_fmac_f32_e32 v136, v68, v200
	v_max_i32_e32 v200, 0, v3
	v_fmac_f32_e32 v135, v68, v200
	v_max_i32_e32 v200, 0, v4
	v_fmac_f32_e32 v134, v68, v200
	v_max_i32_e32 v200, 0, v5
	v_fmac_f32_e32 v65, v68, v200
	v_max_i32_e32 v200, 0, v6
	v_fmac_f32_e32 v64, v68, v200
	v_max_i32_e32 v200, 0, v7
	v_fmac_f32_e32 v63, v68, v200
	v_max_i32_e32 v200, 0, v8
	v_fmac_f32_e32 v62, v68, v200
	v_max_i32_e32 v200, 0, v9
	v_fmac_f32_e32 v61, v68, v200
	v_max_i32_e32 v200, 0, v10
	v_fmac_f32_e32 v60, v68, v200
	v_max_i32_e32 v200, 0, v11
	v_fmac_f32_e32 v59, v68, v200
	v_max_i32_e32 v200, 0, v12
	v_fmac_f32_e32 v58, v68, v200
	v_max_i32_e32 v200, 0, v13
	v_fmac_f32_e32 v57, v68, v200
	v_max_i32_e32 v200, 0, v14
	v_fmac_f32_e32 v56, v68, v200
	v_max_i32_e32 v200, 0, v15
	v_fmac_f32_e32 v55, v68, v200
	v_max_i32_e32 v200, 0, v16
	v_fmac_f32_e32 v54, v68, v200
	v_max_i32_e32 v200, 0, v17
	v_fmac_f32_e32 v53, v68, v200
	v_max_i32_e32 v200, 0, v180
	v_fmac_f32_e32 v136, v69, v200
	v_max_i32_e32 v200, 0, v181
	v_fmac_f32_e32 v135, v69, v200
	v_max_i32_e32 v200, 0, v182
	v_fmac_f32_e32 v134, v69, v200
	v_max_i32_e32 v200, 0, v183
	v_fmac_f32_e32 v65, v69, v200
	v_max_i32_e32 v200, 0, v184
	v_fmac_f32_e32 v64, v69, v200
	v_max_i32_e32 v200, 0, v185
	v_fmac_f32_e32 v63, v69, v200
	v_max_i32_e32 v200, 0, v186
	v_fmac_f32_e32 v62, v69, v200
	v_max_i32_e32 v200, 0, v187
	v_fmac_f32_e32 v61, v69, v200
	v_max_i32_e32 v200, 0, v188
	v_fmac_f32_e32 v60, v69, v200
	v_max_i32_e32 v200, 0, v189
	v_fmac_f32_e32 v59, v69, v200
	v_max_i32_e32 v200, 0, v190
	v_fmac_f32_e32 v58, v69, v200
	v_max_i32_e32 v200, 0, v191
	v_fmac_f32_e32 v57, v69, v200
	v_max_i32_e32 v200, 0, v192
	v_fmac_f32_e32 v56, v69, v200
	v_max_i32_e32 v200, 0, v193
	v_fmac_f32_e32 v55, v69, v200
	v_max_i32_e32 v200, 0, v194
	v_fmac_f32_e32 v54, v69, v200
	v_max_i32_e32 v200, 0, v195
	v_fmac_f32_e32 v53, v69, v200
	s_cbranch_vccz .LBB0_714
; #define LAS __attribute__((address_space(3)))
; __device__ __forceinline__ int crow(int r, int hi) { return (r & 3) + 8 * (r >> 2) + 4 * hi; }
; __device__ __forceinline__ int ibin_u_m160(unsigned u) {
;     const int a = (int)u >> 20;
;     return imed3(-953 - a, 0, 159) + imed3(a - 936, 0, 158) + imed3((int)u, -160, 1);
; }
; template <int PASS, bool DIAG> __device__ __forceinline__ void idx_half(unsigned& bits, unsigned& ebits, const f32x16& sc, int sbase, int tq, int r32, int hi, unsigned khi, unsigned klo, bool cand, LAS unsigned char* L) {
;     bits = 0u; ebits = 0u;
;     const int d = tq - sbase - 4 * hi;
;     if (PASS == 1) {
;         LAS unsigned* H = (LAS unsigned*)(L + IL_HIST) + r32 * HSTR + 160;
; #pragma unroll
;         for (int r = 0; r < 16; ++r) { int b = ibin_u_m160(__float_as_uint(sc[r] + 0.0f)); asm("" : "+v"(b));
;             if (!DIAG || crow(r, 0) <= d) __hip_atomic_fetch_add(H + b, 1u, __ATOMIC_RELAXED, __HIP_MEMORY_SCOPE_WORKGROUP); }
	v_ashrrev_i32_e32 v3, 20, v136
	v_sub_u32_e32 v4, 0xfffffc47, v3
	v_med3_i32 v3, v3, s88, v233
	v_med3_i32 v2, v136, s89, 1
	v_med3_i32 v4, v4, 0, v232
	v_add3_u32 v2, v2, v3, v4
	v_lshl_add_u32 v2, v2, 2, v234
	ds_add_u32 v2, v229 offset:1152
	v_ashrrev_i32_e32 v3, 20, v135
	v_sub_u32_e32 v4, 0xfffffc47, v3
	v_med3_i32 v3, v3, s88, v233
	v_med3_i32 v2, v135, s89, 1
	v_med3_i32 v4, v4, 0, v232
	v_add3_u32 v2, v2, v3, v4
	s_mov_b64 s[16:17], -1
	v_lshl_add_u32 v2, v2, 2, v234
	ds_add_u32 v2, v229 offset:1152
	v_ashrrev_i32_e32 v3, 20, v134
	v_sub_u32_e32 v4, 0xfffffc47, v3
	v_med3_i32 v3, v3, s88, v233
	v_med3_i32 v2, v134, s89, 1
	v_med3_i32 v4, v4, 0, v232
	v_add3_u32 v2, v2, v3, v4
	v_lshl_add_u32 v2, v2, 2, v234
	ds_add_u32 v2, v229 offset:1152
	v_ashrrev_i32_e32 v3, 20, v65
	v_sub_u32_e32 v4, 0xfffffc47, v3
	v_med3_i32 v3, v3, s88, v233
	v_med3_i32 v2, v65, s89, 1
	v_med3_i32 v4, v4, 0, v232
	v_add3_u32 v2, v2, v3, v4
	v_lshl_add_u32 v2, v2, 2, v234
	ds_add_u32 v2, v229 offset:1152
	v_ashrrev_i32_e32 v3, 20, v64
	v_sub_u32_e32 v4, 0xfffffc47, v3
	v_med3_i32 v3, v3, s88, v233
	v_med3_i32 v2, v64, s89, 1
	v_med3_i32 v4, v4, 0, v232
	v_add3_u32 v2, v2, v3, v4
	v_lshl_add_u32 v2, v2, 2, v234
	ds_add_u32 v2, v229 offset:1152
	v_ashrrev_i32_e32 v3, 20, v63
	v_sub_u32_e32 v4, 0xfffffc47, v3
	v_med3_i32 v3, v3, s88, v233
	v_med3_i32 v2, v63, s89, 1
	v_med3_i32 v4, v4, 0, v232
	v_add3_u32 v2, v2, v3, v4
	v_lshl_add_u32 v2, v2, 2, v234
	ds_add_u32 v2, v229 offset:1152
	v_ashrrev_i32_e32 v3, 20, v62
	v_sub_u32_e32 v4, 0xfffffc47, v3
	v_med3_i32 v3, v3, s88, v233
	v_med3_i32 v2, v62, s89, 1
	v_med3_i32 v4, v4, 0, v232
	v_add3_u32 v2, v2, v3, v4
	v_lshl_add_u32 v2, v2, 2, v234
	ds_add_u32 v2, v229 offset:1152
	v_ashrrev_i32_e32 v3, 20, v61
	v_sub_u32_e32 v4, 0xfffffc47, v3
	v_med3_i32 v3, v3, s88, v233
	v_med3_i32 v2, v61, s89, 1
	v_med3_i32 v4, v4, 0, v232
	v_add3_u32 v2, v2, v3, v4
	v_lshl_add_u32 v2, v2, 2, v234
	ds_add_u32 v2, v229 offset:1152
	v_ashrrev_i32_e32 v3, 20, v60
	v_sub_u32_e32 v4, 0xfffffc47, v3
	v_med3_i32 v3, v3, s88, v233
	v_med3_i32 v2, v60, s89, 1
	v_med3_i32 v4, v4, 0, v232
	v_add3_u32 v2, v2, v3, v4
	v_lshl_add_u32 v2, v2, 2, v234
	ds_add_u32 v2, v229 offset:1152
	v_ashrrev_i32_e32 v3, 20, v59
	v_sub_u32_e32 v4, 0xfffffc47, v3
	v_med3_i32 v3, v3, s88, v233
	v_med3_i32 v2, v59, s89, 1
	v_med3_i32 v4, v4, 0, v232
	v_add3_u32 v2, v2, v3, v4
	v_lshl_add_u32 v2, v2, 2, v234
	ds_add_u32 v2, v229 offset:1152
	v_ashrrev_i32_e32 v3, 20, v58
	v_sub_u32_e32 v4, 0xfffffc47, v3
	v_med3_i32 v3, v3, s88, v233
	v_med3_i32 v2, v58, s89, 1
	v_med3_i32 v4, v4, 0, v232
	v_add3_u32 v2, v2, v3, v4
	v_lshl_add_u32 v2, v2, 2, v234
	ds_add_u32 v2, v229 offset:1152
	v_ashrrev_i32_e32 v3, 20, v57
	v_sub_u32_e32 v4, 0xfffffc47, v3
	v_med3_i32 v3, v3, s88, v233
	v_med3_i32 v2, v57, s89, 1
	v_med3_i32 v4, v4, 0, v232
	v_add3_u32 v2, v2, v3, v4
	v_lshl_add_u32 v2, v2, 2, v234
	ds_add_u32 v2, v229 offset:1152
	v_ashrrev_i32_e32 v3, 20, v56
	v_sub_u32_e32 v4, 0xfffffc47, v3
	v_med3_i32 v3, v3, s88, v233
	v_med3_i32 v2, v56, s89, 1
	v_med3_i32 v4, v4, 0, v232
	v_add3_u32 v2, v2, v3, v4
	v_lshl_add_u32 v2, v2, 2, v234
	ds_add_u32 v2, v229 offset:1152
	v_ashrrev_i32_e32 v3, 20, v55
	v_sub_u32_e32 v4, 0xfffffc47, v3
	v_med3_i32 v3, v3, s88, v233
	v_med3_i32 v2, v55, s89, 1
	v_med3_i32 v4, v4, 0, v232
	v_add3_u32 v2, v2, v3, v4
	v_lshl_add_u32 v2, v2, 2, v234
	ds_add_u32 v2, v229 offset:1152
	v_ashrrev_i32_e32 v3, 20, v54
	v_sub_u32_e32 v4, 0xfffffc47, v3
	v_med3_i32 v3, v3, s88, v233
	v_med3_i32 v2, v54, s89, 1
	v_med3_i32 v4, v4, 0, v232
	v_add3_u32 v2, v2, v3, v4
	v_lshl_add_u32 v2, v2, 2, v234
	ds_add_u32 v2, v229 offset:1152
	v_ashrrev_i32_e32 v3, 20, v53
	v_sub_u32_e32 v4, 0xfffffc47, v3
	v_med3_i32 v3, v3, s88, v233
	v_med3_i32 v2, v53, s89, 1
	v_med3_i32 v4, v4, 0, v232
	v_add_u32_e32 v2, v2, v3
	v_add3_u32 v2, v2, v4, s92
	s_cbranch_execz .LBB0_715
	s_branch .LBB0_746

; __device__ __forceinline__ float relu_i(float p) { const int i = __float_as_int(p); return __int_as_float(i > 0 ? i : 0); }
; __device__ __forceinline__ void idx_scores_k(f32x16& sc, const bf16x8 (&kf)[4], const bf16x8 (&qf)[16], const f32x4& w) {
;     f32x16 p0 = f32x16{}, p1 = f32x16{};
; #pragma unroll
;     for (int d0 = 0; d0 < 4; ++d0) p0 = __builtin_amdgcn_mfma_f32_32x32x16_bf16(kf[d0], qf[d0], p0, 0, 0, 0);
; #pragma unroll
;     for (int d0 = 0; d0 < 4; ++d0) p1 = __builtin_amdgcn_mfma_f32_32x32x16_bf16(kf[d0], qf[4 + d0], p1, 0, 0, 0);
; #pragma unroll
;     for (int r = 0; r < 16; ++r) sc[r] = w[0] * relu_i(p0[r]);
;     p0 = f32x16{};
; #pragma unroll
;     for (int d0 = 0; d0 < 4; ++d0) p0 = __builtin_amdgcn_mfma_f32_32x32x16_bf16(kf[d0], qf[8 + d0], p0, 0, 0, 0);
; #pragma unroll
;     for (int r = 0; r < 16; ++r) sc[r] = fmaf(w[1], relu_i(p1[r]), sc[r]);
;     p1 = f32x16{};
; #pragma unroll
;     for (int d0 = 0; d0 < 4; ++d0) p1 = __builtin_amdgcn_mfma_f32_32x32x16_bf16(kf[d0], qf[12 + d0], p1, 0, 0, 0);
; #pragma unroll
;     for (int r = 0; r < 16; ++r) sc[r] = fmaf(w[2], relu_i(p0[r]), sc[r]);
; #pragma unroll
;     for (int r = 0; r < 16; ++r) sc[r] = fmaf(w[3], relu_i(p1[r]), sc[r]);
; }
.LBB0_750:
	s_and_b64 vcc, exec, s[14:15]
	s_waitcnt vmcnt(3)
	v_mfma_f32_32x32x16_bf16 v[2:17], v[46:49], v[70:73], 0
	s_waitcnt vmcnt(2)
	v_mfma_f32_32x32x16_bf16 v[2:17], v[42:45], v[74:77], v[2:17]
	s_waitcnt vmcnt(1)
	v_mfma_f32_32x32x16_bf16 v[2:17], v[38:41], v[78:81], v[2:17]
	s_waitcnt vmcnt(0)
	v_mfma_f32_32x32x16_bf16 v[2:17], v[34:37], v[82:85], v[2:17]
	v_mfma_f32_32x32x16_bf16 v[180:195], v[46:49], v[86:89], 0
	v_mfma_f32_32x32x16_bf16 v[180:195], v[42:45], v[90:93], v[180:195]
	v_mfma_f32_32x32x16_bf16 v[180:195], v[38:41], v[94:97], v[180:195]
	v_mfma_f32_32x32x16_bf16 v[180:195], v[34:37], v[98:101], v[180:195]
	s_nop 7
	v_max_i32_e32 v200, 0, v2
	v_fma_f32 v136, v66, v200, 0
	v_max_i32_e32 v200, 0, v3
	v_fma_f32 v135, v66, v200, 0
	v_max_i32_e32 v200, 0, v4
	v_fma_f32 v134, v66, v200, 0
	v_max_i32_e32 v200, 0, v5
	v_fma_f32 v65, v66, v200, 0
	v_max_i32_e32 v200, 0, v6
	v_fma_f32 v64, v66, v200, 0
	v_max_i32_e32 v200, 0, v7
	v_fma_f32 v63, v66, v200, 0
	v_max_i32_e32 v200, 0, v8
	v_fma_f32 v62, v66, v200, 0
	v_max_i32_e32 v200, 0, v9
	v_fma_f32 v61, v66, v200, 0
	v_max_i32_e32 v200, 0, v10
	v_fma_f32 v60, v66, v200, 0
	v_max_i32_e32 v200, 0, v11
	v_fma_f32 v59, v66, v200, 0
	v_max_i32_e32 v200, 0, v12
	v_fma_f32 v58, v66, v200, 0
	v_max_i32_e32 v200, 0, v13
	v_fma_f32 v57, v66, v200, 0
	v_max_i32_e32 v200, 0, v14
	v_fma_f32 v56, v66, v200, 0
	v_max_i32_e32 v200, 0, v15
	v_fma_f32 v55, v66, v200, 0
	v_max_i32_e32 v200, 0, v16
	v_fma_f32 v54, v66, v200, 0
	v_max_i32_e32 v200, 0, v17
	v_fma_f32 v53, v66, v200, 0
	v_mfma_f32_32x32x16_bf16 v[2:17], v[46:49], v[102:105], 0
	v_mfma_f32_32x32x16_bf16 v[2:17], v[42:45], v[106:109], v[2:17]
	v_mfma_f32_32x32x16_bf16 v[2:17], v[38:41], v[110:113], v[2:17]
	v_mfma_f32_32x32x16_bf16 v[2:17], v[34:37], v[114:117], v[2:17]
	v_max_i32_e32 v200, 0, v180
	v_fmac_f32_e32 v136, v67, v200
	v_max_i32_e32 v200, 0, v181
	v_fmac_f32_e32 v135, v67, v200
	v_max_i32_e32 v200, 0, v182
	v_fmac_f32_e32 v134, v67, v200
	v_max_i32_e32 v200, 0, v183
	v_fmac_f32_e32 v65, v67, v200
	v_max_i32_e32 v200, 0, v184
	v_fmac_f32_e32 v64, v67, v200
	v_max_i32_e32 v200, 0, v185
	v_fmac_f32_e32 v63, v67, v200
	v_max_i32_e32 v200, 0, v186
	v_fmac_f32_e32 v62, v67, v200
	v_max_i32_e32 v200, 0, v187
	v_fmac_f32_e32 v61, v67, v200
	v_max_i32_e32 v200, 0, v188
	v_fmac_f32_e32 v60, v67, v200
	v_max_i32_e32 v200, 0, v189
	v_fmac_f32_e32 v59, v67, v200
	v_max_i32_e32 v200, 0, v190
	v_fmac_f32_e32 v58, v67, v200
	v_max_i32_e32 v200, 0, v191
	v_fmac_f32_e32 v57, v67, v200
	v_max_i32_e32 v200, 0, v192
	v_fmac_f32_e32 v56, v67, v200
	v_max_i32_e32 v200, 0, v193
	v_fmac_f32_e32 v55, v67, v200
	v_max_i32_e32 v200, 0, v194
	v_fmac_f32_e32 v54, v67, v200
	v_max_i32_e32 v200, 0, v195
	v_fmac_f32_e32 v53, v67, v200
	v_mfma_f32_32x32x16_bf16 v[180:195], v[46:49], v[118:121], 0
	v_mfma_f32_32x32x16_bf16 v[180:195], v[42:45], v[122:125], v[180:195]
	v_mfma_f32_32x32x16_bf16 v[180:195], v[38:41], v[126:129], v[180:195]
	v_mfma_f32_32x32x16_bf16 v[180:195], v[34:37], v[130:133], v[180:195]
	v_max_i32_e32 v200, 0, v2
	v_fmac_f32_e32 v136, v68, v200
	v_max_i32_e32 v200, 0, v3
	v_fmac_f32_e32 v135, v68, v200
	v_max_i32_e32 v200, 0, v4
	v_fmac_f32_e32 v134, v68, v200
	v_max_i32_e32 v200, 0, v5
	v_fmac_f32_e32 v65, v68, v200
	v_max_i32_e32 v200, 0, v6
	v_fmac_f32_e32 v64, v68, v200
	v_max_i32_e32 v200, 0, v7
	v_fmac_f32_e32 v63, v68, v200
	v_max_i32_e32 v200, 0, v8
	v_fmac_f32_e32 v62, v68, v200
	v_max_i32_e32 v200, 0, v9
	v_fmac_f32_e32 v61, v68, v200
	v_max_i32_e32 v200, 0, v10
	v_fmac_f32_e32 v60, v68, v200
	v_max_i32_e32 v200, 0, v11
	v_fmac_f32_e32 v59, v68, v200
	v_max_i32_e32 v200, 0, v12
	v_fmac_f32_e32 v58, v68, v200
	v_max_i32_e32 v200, 0, v13
	v_fmac_f32_e32 v57, v68, v200
	v_max_i32_e32 v200, 0, v14
	v_fmac_f32_e32 v56, v68, v200
	v_max_i32_e32 v200, 0, v15
	v_fmac_f32_e32 v55, v68, v200
	v_max_i32_e32 v200, 0, v16
	v_fmac_f32_e32 v54, v68, v200
	v_max_i32_e32 v200, 0, v17
	v_fmac_f32_e32 v53, v68, v200
	v_max_i32_e32 v200, 0, v180
	v_fmac_f32_e32 v136, v69, v200
	v_max_i32_e32 v200, 0, v181
	v_fmac_f32_e32 v135, v69, v200
	v_max_i32_e32 v200, 0, v182
	v_fmac_f32_e32 v134, v69, v200
	v_max_i32_e32 v200, 0, v183
	v_fmac_f32_e32 v65, v69, v200
	v_max_i32_e32 v200, 0, v184
	v_fmac_f32_e32 v64, v69, v200
	v_max_i32_e32 v200, 0, v185
	v_fmac_f32_e32 v63, v69, v200
	v_max_i32_e32 v200, 0, v186
	v_fmac_f32_e32 v62, v69, v200
	v_max_i32_e32 v200, 0, v187
	v_fmac_f32_e32 v61, v69, v200
	v_max_i32_e32 v200, 0, v188
	v_fmac_f32_e32 v60, v69, v200
	v_max_i32_e32 v200, 0, v189
	v_fmac_f32_e32 v59, v69, v200
	v_max_i32_e32 v200, 0, v190
	v_fmac_f32_e32 v58, v69, v200
	v_max_i32_e32 v200, 0, v191
	v_fmac_f32_e32 v57, v69, v200
	v_max_i32_e32 v200, 0, v192
	v_fmac_f32_e32 v56, v69, v200
	v_max_i32_e32 v200, 0, v193
	v_fmac_f32_e32 v55, v69, v200
	v_max_i32_e32 v200, 0, v194
	v_fmac_f32_e32 v54, v69, v200
	v_max_i32_e32 v200, 0, v195
	v_fmac_f32_e32 v53, v69, v200
	s_cbranch_vccz .LBB0_752
; #define LAS __attribute__((address_space(3)))
; __device__ __forceinline__ int crow(int r, int hi) { return (r & 3) + 8 * (r >> 2) + 4 * hi; }
; __device__ __forceinline__ int ibin_u_m160(unsigned u) {
;     const int a = (int)u >> 20;
;     return imed3(-953 - a, 0, 159) + imed3(a - 936, 0, 158) + imed3((int)u, -160, 1);
; }
; template <int PASS, bool DIAG> __device__ __forceinline__ void idx_half(unsigned& bits, unsigned& ebits, const f32x16& sc, int sbase, int tq, int r32, int hi, unsigned khi, unsigned klo, bool cand, LAS unsigned char* L) {
;     bits = 0u; ebits = 0u;
;     const int d = tq - sbase - 4 * hi;
;     if (PASS == 1) {
;         LAS unsigned* H = (LAS unsigned*)(L + IL_HIST) + r32 * HSTR + 160;
; #pragma unroll
;         for (int r = 0; r < 16; ++r) { int b = ibin_u_m160(__float_as_uint(sc[r] + 0.0f)); asm("" : "+v"(b));
;             if (!DIAG || crow(r, 0) <= d) __hip_atomic_fetch_add(H + b, 1u, __ATOMIC_RELAXED, __HIP_MEMORY_SCOPE_WORKGROUP); }
	v_ashrrev_i32_e32 v3, 20, v136
	v_sub_u32_e32 v4, 0xfffffc47, v3
	v_med3_i32 v3, v3, s88, v233
	v_med3_i32 v2, v136, s89, 1
	v_med3_i32 v4, v4, 0, v232
	v_add3_u32 v2, v2, v3, v4
	v_lshl_add_u32 v2, v2, 2, v234
	ds_add_u32 v2, v229 offset:1152
	v_ashrrev_i32_e32 v3, 20, v135
	v_sub_u32_e32 v4, 0xfffffc47, v3
	v_med3_i32 v3, v3, s88, v233
	v_med3_i32 v2, v135, s89, 1
	v_med3_i32 v4, v4, 0, v232
	v_add_u32_e32 v2, v2, v3
	v_add3_u32 v2, v2, v4, s92
	s_mov_b64 s[14:15], -1
	v_lshl_add_u32 v2, v2, 2, v0
	ds_add_u32 v2, v229 offset:1152
	v_ashrrev_i32_e32 v3, 20, v134
	v_sub_u32_e32 v4, 0xfffffc47, v3
	v_med3_i32 v3, v3, s88, v233
	v_med3_i32 v2, v134, s89, 1
	v_med3_i32 v4, v4, 0, v232
	v_add3_u32 v2, v2, v3, v4
	v_lshl_add_u32 v2, v2, 2, v234
	ds_add_u32 v2, v229 offset:1152
	v_ashrrev_i32_e32 v3, 20, v65
	v_sub_u32_e32 v4, 0xfffffc47, v3
	v_med3_i32 v3, v3, s88, v233
	v_med3_i32 v2, v65, s89, 1
	v_med3_i32 v4, v4, 0, v232
	v_add3_u32 v2, v2, v3, v4
	v_lshl_add_u32 v2, v2, 2, v234
	ds_add_u32 v2, v229 offset:1152
	v_ashrrev_i32_e32 v3, 20, v64
	v_sub_u32_e32 v4, 0xfffffc47, v3
	v_med3_i32 v3, v3, s88, v233
	v_med3_i32 v2, v64, s89, 1
	v_med3_i32 v4, v4, 0, v232
	v_add3_u32 v2, v2, v3, v4
	v_lshl_add_u32 v2, v2, 2, v234
	ds_add_u32 v2, v229 offset:1152
	v_ashrrev_i32_e32 v3, 20, v63
	v_sub_u32_e32 v4, 0xfffffc47, v3
	v_med3_i32 v3, v3, s88, v233
	v_med3_i32 v2, v63, s89, 1
	v_med3_i32 v4, v4, 0, v232
	v_add3_u32 v2, v2, v3, v4
	v_lshl_add_u32 v2, v2, 2, v234
	ds_add_u32 v2, v229 offset:1152
	v_ashrrev_i32_e32 v3, 20, v62
	v_sub_u32_e32 v4, 0xfffffc47, v3
	v_med3_i32 v3, v3, s88, v233
	v_med3_i32 v2, v62, s89, 1
	v_med3_i32 v4, v4, 0, v232
	v_add3_u32 v2, v2, v3, v4
	v_lshl_add_u32 v2, v2, 2, v234
	ds_add_u32 v2, v229 offset:1152
	v_ashrrev_i32_e32 v3, 20, v61
	v_sub_u32_e32 v4, 0xfffffc47, v3
	v_med3_i32 v3, v3, s88, v233
	v_med3_i32 v2, v61, s89, 1
	v_med3_i32 v4, v4, 0, v232
	v_add3_u32 v2, v2, v3, v4
	v_lshl_add_u32 v2, v2, 2, v234
	ds_add_u32 v2, v229 offset:1152
	v_ashrrev_i32_e32 v3, 20, v60
	v_sub_u32_e32 v4, 0xfffffc47, v3
	v_med3_i32 v3, v3, s88, v233
	v_med3_i32 v2, v60, s89, 1
	v_med3_i32 v4, v4, 0, v232
	v_add3_u32 v2, v2, v3, v4
	v_lshl_add_u32 v2, v2, 2, v234
	ds_add_u32 v2, v229 offset:1152
	v_ashrrev_i32_e32 v3, 20, v59
	v_sub_u32_e32 v4, 0xfffffc47, v3
	v_med3_i32 v3, v3, s88, v233
	v_med3_i32 v2, v59, s89, 1
	v_med3_i32 v4, v4, 0, v232
	v_add3_u32 v2, v2, v3, v4
	v_lshl_add_u32 v2, v2, 2, v234
	ds_add_u32 v2, v229 offset:1152
	v_ashrrev_i32_e32 v3, 20, v58
	v_sub_u32_e32 v4, 0xfffffc47, v3
	v_med3_i32 v3, v3, s88, v233
	v_med3_i32 v2, v58, s89, 1
	v_med3_i32 v4, v4, 0, v232
	v_add3_u32 v2, v2, v3, v4
	v_lshl_add_u32 v2, v2, 2, v234
	ds_add_u32 v2, v229 offset:1152
	v_ashrrev_i32_e32 v3, 20, v57
	v_sub_u32_e32 v4, 0xfffffc47, v3
	v_med3_i32 v3, v3, s88, v233
	v_med3_i32 v2, v57, s89, 1
	v_med3_i32 v4, v4, 0, v232
	v_add3_u32 v2, v2, v3, v4
	v_lshl_add_u32 v2, v2, 2, v234
	ds_add_u32 v2, v229 offset:1152
	v_ashrrev_i32_e32 v3, 20, v56
	v_sub_u32_e32 v4, 0xfffffc47, v3
	v_med3_i32 v3, v3, s88, v233
	v_med3_i32 v2, v56, s89, 1
	v_med3_i32 v4, v4, 0, v232
	v_add3_u32 v2, v2, v3, v4
	v_lshl_add_u32 v2, v2, 2, v234
	ds_add_u32 v2, v229 offset:1152
	v_ashrrev_i32_e32 v3, 20, v55
	v_sub_u32_e32 v4, 0xfffffc47, v3
	v_med3_i32 v3, v3, s88, v233
	v_med3_i32 v2, v55, s89, 1
	v_med3_i32 v4, v4, 0, v232
	v_add3_u32 v2, v2, v3, v4
	v_lshl_add_u32 v2, v2, 2, v234
	ds_add_u32 v2, v229 offset:1152
	v_ashrrev_i32_e32 v3, 20, v54
	v_sub_u32_e32 v4, 0xfffffc47, v3
	v_med3_i32 v3, v3, s88, v233
	v_med3_i32 v2, v54, s89, 1
	v_med3_i32 v4, v4, 0, v232
	v_add3_u32 v2, v2, v3, v4
	v_lshl_add_u32 v2, v2, 2, v234
	ds_add_u32 v2, v229 offset:1152
	v_ashrrev_i32_e32 v3, 20, v53
	v_sub_u32_e32 v4, 0xfffffc47, v3
	v_med3_i32 v3, v3, s88, v233
	v_med3_i32 v2, v53, s89, 1
	v_med3_i32 v4, v4, 0, v232
	v_add_u32_e32 v2, v2, v3
	v_add3_u32 v3, v2, v4, s92
	s_cbranch_execz .LBB0_753
	s_branch .LBB0_784

; __device__ __forceinline__ void glds16_s(const void* sbase  , unsigned voff  , unsigned lds_dst  ) {
;     unsigned keep;
;     asm volatile("s_nop 4\n\ts_mov_b32 %0, m0\n\ts_mov_b32 m0, %3\n\ts_nop 0\n\tglobal_load_lds_dwordx4 %1, %2\n\ts_mov_b32 m0, %0" : "=&s"(keep) : "v"(voff), "s"(sbase), "s"(lds_dst) : "memory");
; }
; __device__ __forceinline__ void dsa_block_unit(int b, int g, int m  , const bf16_t* Q, const bf16_t* K, const bf16_t* V, const unsigned long long* mask, bf16_t* O, LAS char* L, int wid, int lane, float sbound  ) {
;     ...
;         if (j + 2 <= jd) { glds16_s(Kw + (size_t)(j + 2) * 64 * 128, kvoff, kdst + sn2); glds16_s(Vw + (size_t)(j + 2) * 64 * 128, vvoff, vdst + sn2); mwn2 = mrow[j + 2]; }
.LBB0_1684:
	s_add_i32 s60, s58, -1
	s_mov_b32 s59, s0
	s_cmp_gt_u32 s60, s54
	s_waitcnt vmcnt(0)
	v_mov_b64_e32 v[170:171], v[116:117]
	s_cbranch_scc1 .LBB0_1686
	s_add_u32 s0, s16, s30
	s_addc_u32 s1, s17, s31
	s_add_u32 s0, s0, 0x8000
	s_addc_u32 s1, s1, 0
	s_add_i32 s33, s59, s63
	s_add_u32 s2, s18, s30
	s_addc_u32 s3, s19, s31
	s_add_u32 s2, s2, 0x8000
	s_mov_b32 s35, m0
	s_mov_b32 m0, s33
	s_nop 0
	global_load_lds_dwordx4 v172, s[0:1]
	s_mov_b32 m0, s35
	s_addc_u32 s3, s3, 0
	s_add_i32 s34, s59, s64
	s_mov_b32 s0, m0
	s_mov_b32 m0, s34
	s_nop 0
	global_load_lds_dwordx4 v173, s[2:3]
	s_mov_b32 m0, s0
	global_load_dwordx2 v[170:171], v[168:169], off offset:-8 sc1

; #define LDS_WAIT() asm volatile("s_waitcnt lgkmcnt(0)" ::: "memory")
; __device__ __forceinline__ int crow(int r, int hi) { return (r & 3) + 8 * (r >> 2) + 4 * hi; }
; __device__ __forceinline__ void dsa_step(f32x16& c0, f32x16& c1, f32x16& n0, f32x16& n1, const bool have_n, const LAS char* kpn, const LAS char* vpc, const bf16x8 (&qr)[4], unsigned long long mwn, ...
;     ...
;     f32x2 ps2 = {0.f, 0.f};
; #pragma unroll
;     for (int r = 0; r < 16; r += 2) { c0[r] = __builtin_amdgcn_exp2f(c0[r]); c0[r + 1] = __builtin_amdgcn_exp2f(c0[r + 1]); c1[r] = __builtin_amdgcn_exp2f(c1[r]); c1[r + 1] = __builtin_amdgcn_exp2f(c1[r + 1]);
;         ps2 += (f32x2){c0[r], c0[r + 1]}; ps2 += (f32x2){c1[r], c1[r + 1]}; }
;     lsum += ps2[0] + ps2[1];
;     if (resc) { LDS_WAIT();
; #pragma unroll
;         for (int r = 0; r < 16; ++r) { const float f = wsf[crow(r, hi)]; o[0][r] *= f; o[1][r] *= f; } }
;     pv_mma(o, vf, c0, c1);
;     asm volatile("s_waitcnt vmcnt(0) lgkmcnt(0)\n\ts_barrier" ::: "memory");
; __device__ __forceinline__ void dsa_block_unit(int b, int g, int m  , const bf16_t* Q, const bf16_t* K, const bf16_t* V, const unsigned long long* mask, bf16_t* O, LAS char* L, int wid, int lane, float sbound  ) {
;     ...
;         if (j + 3 <= jd) { glds16_s(Kw + (size_t)(j + 3) * 64 * 128, kvoff, kdst + sn2); glds16_s(Vw + (size_t)(j + 3) * 64 * 128, vvoff, vdst + sn2); mwn2 = mrow[j + 3]; }
.LBB0_1696:
	s_or_b64 exec, exec, s[34:35]
	v_exp_f32_e32 v34, v34
	v_exp_f32_e32 v35, v35
	v_exp_f32_e32 v36, v36
	v_exp_f32_e32 v37, v37
	v_exp_f32_e32 v38, v38
	v_exp_f32_e32 v39, v39
	v_exp_f32_e32 v40, v40
	v_exp_f32_e32 v41, v41
	v_cvt_pk_bf16_f32 v146, v34, v35
	v_cvt_pk_bf16_f32 v147, v36, v37
	v_cvt_pk_bf16_f32 v148, v38, v39
	v_cvt_pk_bf16_f32 v149, v40, v41
	v_exp_f32_e32 v42, v42
	v_exp_f32_e32 v43, v43
	v_exp_f32_e32 v44, v44
	v_exp_f32_e32 v45, v45
	v_exp_f32_e32 v46, v46
	v_exp_f32_e32 v47, v47
	v_exp_f32_e32 v48, v48
	v_exp_f32_e32 v49, v49
	s_waitcnt lgkmcnt(14)
	v_mfma_f32_32x32x16_bf16 v[2:17], v[146:149], v[142:145], v[2:17]
	v_exp_f32_e32 v50, v50
	v_exp_f32_e32 v51, v51
	v_cvt_pk_bf16_f32 v142, v42, v43
	v_cvt_pk_bf16_f32 v143, v44, v45
	v_cvt_pk_bf16_f32 v144, v46, v47
	v_cvt_pk_bf16_f32 v145, v48, v49
	v_exp_f32_e32 v52, v52
	s_waitcnt lgkmcnt(10)
	v_mfma_f32_32x32x16_bf16 v[18:33], v[146:149], v[138:141], v[18:33]
	v_exp_f32_e32 v53, v53
	v_pk_add_f32 v[186:187], v[34:35], 0 op_sel_hi:[1,0]
	v_exp_f32_e32 v54, v54
	v_pk_add_f32 v[186:187], v[50:51], v[186:187]
	v_exp_f32_e32 v55, v55
	v_exp_f32_e32 v56, v56
	v_exp_f32_e32 v57, v57
	v_mfma_f32_32x32x16_bf16 v[2:17], v[142:145], v[134:137], v[2:17]
	v_add_f32_e64 v134, v186, v36
	v_add_f32_e64 v135, v187, v37
	v_cvt_pk_bf16_f32 v136, v54, v55
	v_add_f32_e64 v134, v52, v134
	v_add_f32_e64 v135, v53, v135
	v_cvt_pk_bf16_f32 v137, v56, v57
	v_pk_add_f32 v[134:135], v[134:135], v[38:39]
	v_exp_f32_e32 v58, v58
	v_pk_add_f32 v[138:139], v[54:55], v[134:135]
	s_waitcnt lgkmcnt(8)
	v_mfma_f32_32x32x16_bf16 v[18:33], v[142:145], v[130:133], v[18:33]
	v_cvt_pk_bf16_f32 v134, v50, v51
	v_cvt_pk_bf16_f32 v135, v52, v53
	v_exp_f32_e32 v59, v59
	v_exp_f32_e32 v60, v60
	v_exp_f32_e32 v61, v61
	v_exp_f32_e32 v62, v62
	v_exp_f32_e32 v63, v63
	v_exp_f32_e32 v64, v64
	v_exp_f32_e32 v65, v65
	s_waitcnt lgkmcnt(6)
	v_mfma_f32_32x32x16_bf16 v[2:17], v[134:137], v[126:129], v[2:17]
	v_cvt_pk_bf16_f32 v126, v58, v59
	v_cvt_pk_bf16_f32 v127, v60, v61
	v_cvt_pk_bf16_f32 v128, v62, v63
	v_cvt_pk_bf16_f32 v129, v64, v65
	v_add_f32_e64 v130, v138, v40
	v_add_f32_e64 v131, v139, v41
	s_waitcnt vmcnt(0) lgkmcnt(0)
	s_barrier
	s_add_i32 s0, s21, s58
	s_waitcnt lgkmcnt(2)
	v_mfma_f32_32x32x16_bf16 v[18:33], v[134:137], v[122:125], v[18:33]
	v_add_f32_e64 v130, v56, v130
	v_add_f32_e64 v131, v57, v131
	s_cmp_eq_u32 s0, 3
	v_add_f32_e64 v122, v130, v42
	v_add_f32_e64 v123, v131, v43
	v_readfirstlane_b32 s36, v0
	v_pk_add_f32 v[122:123], v[58:59], v[122:123]
	v_readfirstlane_b32 s37, v1
	v_pk_add_f32 v[122:123], v[122:123], v[44:45]
	v_mfma_f32_32x32x16_bf16 v[2:17], v[126:129], v[118:121], v[2:17]
	v_add_f32_e64 v122, v60, v122
	v_add_f32_e64 v123, v61, v123
	v_add_f32_e64 v118, v122, v46
	v_add_f32_e64 v119, v123, v47
	v_add_f32_e64 v118, v62, v118
	v_add_f32_e64 v119, v63, v119
	v_pk_add_f32 v[118:119], v[118:119], v[48:49]
	s_waitcnt lgkmcnt(0)
	v_mfma_f32_32x32x16_bf16 v[18:33], v[126:129], v[114:117], v[18:33]
	v_add_f32_e64 v118, v64, v118
	v_add_f32_e64 v119, v65, v119
	v_add_f32_e32 v118, v118, v119
	v_add_f32_e32 v157, v157, v118
	s_cbranch_scc1 .LBB0_1682
	s_cmp_gt_u32 s58, s54
	s_waitcnt vmcnt(0)
	v_mov_b64_e32 v[116:117], v[170:171]
	s_cbranch_scc1 .LBB0_1699
	s_add_u32 s0, s16, s30
	s_addc_u32 s1, s17, s31
	s_add_u32 s0, s0, 0xc000
	s_addc_u32 s1, s1, 0
	s_add_i32 s33, s55, s63
	s_add_u32 s2, s18, s30
	s_addc_u32 s3, s19, s31
	s_add_u32 s2, s2, 0xc000
	s_mov_b32 s35, m0
	s_mov_b32 m0, s33
	s_nop 0
	global_load_lds_dwordx4 v172, s[0:1]
	s_mov_b32 m0, s35
	s_addc_u32 s3, s3, 0
	s_add_i32 s34, s55, s64
	s_mov_b32 s0, m0
	s_mov_b32 m0, s34
	s_nop 0
	global_load_lds_dwordx4 v173, s[2:3]
	s_mov_b32 m0, s0
	global_load_dwordx2 v[116:117], v[168:169], off sc1

; __device__ __forceinline__ void glds16_s(const void* sbase  , unsigned voff  , unsigned lds_dst  ) {
;     unsigned keep;
;     asm volatile("s_nop 4\n\ts_mov_b32 %0, m0\n\ts_mov_b32 m0, %3\n\ts_nop 0\n\tglobal_load_lds_dwordx4 %1, %2\n\ts_mov_b32 m0, %0" : "=&s"(keep) : "v"(voff), "s"(sbase), "s"(lds_dst) : "memory");
; }
; __device__ __forceinline__ void dsa_block_unit(int b, int g, int m  , const bf16_t* Q, const bf16_t* K, const bf16_t* V, const unsigned long long* mask, bf16_t* O, LAS char* L, int wid, int lane, float sbound  ) {
;     ...
;         if (j + 2 <= jd) { glds16_s(Kw + (size_t)(j + 2) * 64 * 128, kvoff, kdst + sn2); glds16_s(Vw + (size_t)(j + 2) * 64 * 128, vvoff, vdst + sn2); mwn2 = mrow[j + 2]; }
.LBB0_1755:
	s_add_i32 s37, s35, -1
	s_mov_b32 s36, s0
	s_cmp_gt_u32 s37, s53
	s_waitcnt vmcnt(0)
	v_mov_b64_e32 v[166:167], v[148:149]
	s_cbranch_scc1 .LBB0_1757
	s_add_u32 s0, s16, s20
	s_addc_u32 s1, s17, s21
	s_add_u32 s0, s0, 0x8000
	s_addc_u32 s1, s1, 0
	s_add_i32 s22, s36, s63
	s_add_u32 s2, s18, s20
	s_addc_u32 s3, s19, s21
	s_add_u32 s2, s2, 0x8000
	s_mov_b32 s24, m0
	s_mov_b32 m0, s22
	s_nop 0
	global_load_lds_dwordx4 v172, s[0:1]
	s_mov_b32 m0, s24
	s_addc_u32 s3, s3, 0
	s_add_i32 s23, s36, s64
	s_mov_b32 s0, m0
	s_mov_b32 m0, s23
	s_nop 0
	global_load_lds_dwordx4 v173, s[2:3]
	s_mov_b32 m0, s0
	global_load_dwordx2 v[166:167], v[146:147], off offset:-8 sc1

; #define LDS_WAIT() asm volatile("s_waitcnt lgkmcnt(0)" ::: "memory")
; __device__ __forceinline__ int crow(int r, int hi) { return (r & 3) + 8 * (r >> 2) + 4 * hi; }
; __device__ __forceinline__ void dsa_step(f32x16& c0, f32x16& c1, f32x16& n0, f32x16& n1, const bool have_n, const LAS char* kpn, const LAS char* vpc, const bf16x8 (&qr)[4], unsigned long long mwn, ...
;     ...
;     f32x2 ps2 = {0.f, 0.f};
; #pragma unroll
;     for (int r = 0; r < 16; r += 2) { c0[r] = __builtin_amdgcn_exp2f(c0[r]); c0[r + 1] = __builtin_amdgcn_exp2f(c0[r + 1]); c1[r] = __builtin_amdgcn_exp2f(c1[r]); c1[r + 1] = __builtin_amdgcn_exp2f(c1[r + 1]);
;         ps2 += (f32x2){c0[r], c0[r + 1]}; ps2 += (f32x2){c1[r], c1[r + 1]}; }
;     lsum += ps2[0] + ps2[1];
;     if (resc) { LDS_WAIT();
; #pragma unroll
;         for (int r = 0; r < 16; ++r) { const float f = wsf[crow(r, hi)]; o[0][r] *= f; o[1][r] *= f; } }
;     pv_mma(o, vf, c0, c1);
;     asm volatile("s_waitcnt vmcnt(0) lgkmcnt(0)\n\ts_barrier" ::: "memory");
; __device__ __forceinline__ void dsa_block_unit(int b, int g, int m  , const bf16_t* Q, const bf16_t* K, const bf16_t* V, const unsigned long long* mask, bf16_t* O, LAS char* L, int wid, int lane, float sbound  ) {
;     ...
;         if (j + 3 <= jd) { glds16_s(Kw + (size_t)(j + 3) * 64 * 128, kvoff, kdst + sn2); glds16_s(Vw + (size_t)(j + 3) * 64 * 128, vvoff, vdst + sn2); mwn2 = mrow[j + 3]; }
.LBB0_1767:
	s_or_b64 exec, exec, s[22:23]
	v_exp_f32_e32 v34, v34
	v_exp_f32_e32 v35, v35
	v_exp_f32_e32 v36, v36
	v_exp_f32_e32 v37, v37
	v_exp_f32_e32 v38, v38
	v_exp_f32_e32 v39, v39
	v_exp_f32_e32 v40, v40
	v_exp_f32_e32 v41, v41
	v_cvt_pk_bf16_f32 v186, v34, v35
	v_cvt_pk_bf16_f32 v187, v36, v37
	v_cvt_pk_bf16_f32 v188, v38, v39
	v_cvt_pk_bf16_f32 v189, v40, v41
	v_exp_f32_e32 v42, v42
	v_exp_f32_e32 v43, v43
	v_exp_f32_e32 v44, v44
	v_exp_f32_e32 v45, v45
	v_exp_f32_e32 v46, v46
	v_exp_f32_e32 v47, v47
	v_exp_f32_e32 v48, v48
	v_exp_f32_e32 v49, v49
	s_waitcnt lgkmcnt(14)
	v_mfma_f32_32x32x16_bf16 v[18:33], v[186:189], v[142:145], v[18:33]
	v_exp_f32_e32 v50, v50
	v_exp_f32_e32 v51, v51
	v_cvt_pk_bf16_f32 v142, v42, v43
	v_cvt_pk_bf16_f32 v143, v44, v45
	v_cvt_pk_bf16_f32 v144, v46, v47
	v_cvt_pk_bf16_f32 v145, v48, v49
	v_exp_f32_e32 v52, v52
	s_waitcnt lgkmcnt(10)
	v_mfma_f32_32x32x16_bf16 v[2:17], v[186:189], v[138:141], v[2:17]
	v_exp_f32_e32 v53, v53
	v_pk_add_f32 v[148:149], v[34:35], 0 op_sel_hi:[1,0]
	v_exp_f32_e32 v54, v54
	v_pk_add_f32 v[148:149], v[50:51], v[148:149]
	v_exp_f32_e32 v55, v55
	v_exp_f32_e32 v56, v56
	v_exp_f32_e32 v57, v57
	v_mfma_f32_32x32x16_bf16 v[18:33], v[142:145], v[134:137], v[18:33]
	v_add_f32_e64 v134, v148, v36
	v_add_f32_e64 v135, v149, v37
	v_cvt_pk_bf16_f32 v136, v54, v55
	v_add_f32_e64 v134, v52, v134
	v_add_f32_e64 v135, v53, v135
	v_cvt_pk_bf16_f32 v137, v56, v57
	v_pk_add_f32 v[134:135], v[134:135], v[38:39]
	v_exp_f32_e32 v58, v58
	v_pk_add_f32 v[138:139], v[54:55], v[134:135]
	s_waitcnt lgkmcnt(8)
	v_mfma_f32_32x32x16_bf16 v[2:17], v[142:145], v[130:133], v[2:17]
	v_cvt_pk_bf16_f32 v134, v50, v51
	v_cvt_pk_bf16_f32 v135, v52, v53
	v_exp_f32_e32 v59, v59
	v_exp_f32_e32 v60, v60
	v_exp_f32_e32 v61, v61
	v_exp_f32_e32 v62, v62
	v_exp_f32_e32 v63, v63
	v_exp_f32_e32 v64, v64
	v_exp_f32_e32 v65, v65
	s_waitcnt lgkmcnt(6)
	v_mfma_f32_32x32x16_bf16 v[18:33], v[134:137], v[126:129], v[18:33]
	v_cvt_pk_bf16_f32 v126, v58, v59
	v_cvt_pk_bf16_f32 v127, v60, v61
	v_cvt_pk_bf16_f32 v128, v62, v63
	v_cvt_pk_bf16_f32 v129, v64, v65
	v_add_f32_e64 v130, v138, v40
	v_add_f32_e64 v131, v139, v41
	s_waitcnt vmcnt(0) lgkmcnt(0)
	s_barrier
	s_add_i32 s0, s30, s35
	s_waitcnt lgkmcnt(2)
	v_mfma_f32_32x32x16_bf16 v[2:17], v[134:137], v[122:125], v[2:17]
	v_add_f32_e64 v130, v56, v130
	v_add_f32_e64 v131, v57, v131
	s_cmp_eq_u32 s0, 3
	v_add_f32_e64 v122, v130, v42
	v_add_f32_e64 v123, v131, v43
	v_readfirstlane_b32 s25, v1
	v_pk_add_f32 v[122:123], v[58:59], v[122:123]
	s_nop 0
	v_pk_add_f32 v[122:123], v[122:123], v[44:45]
	v_mfma_f32_32x32x16_bf16 v[18:33], v[126:129], v[118:121], v[18:33]
	v_add_f32_e64 v122, v60, v122
	v_add_f32_e64 v123, v61, v123
	v_add_f32_e64 v118, v122, v46
	v_add_f32_e64 v119, v123, v47
	v_add_f32_e64 v118, v62, v118
	v_add_f32_e64 v119, v63, v119
	v_pk_add_f32 v[118:119], v[118:119], v[48:49]
	s_waitcnt lgkmcnt(0)
	v_mfma_f32_32x32x16_bf16 v[2:17], v[126:129], v[114:117], v[2:17]
	v_add_f32_e64 v118, v64, v118
	v_add_f32_e64 v119, v65, v119
	v_add_f32_e32 v0, v118, v119
	v_add_f32_e32 v157, v157, v0
	v_readfirstlane_b32 s24, v0
	s_cbranch_scc1 .LBB0_1753
	s_cmp_gt_u32 s35, s53
	s_waitcnt vmcnt(0)
	v_mov_b64_e32 v[148:149], v[166:167]
	s_cbranch_scc1 .LBB0_1770
	s_add_u32 s0, s16, s20
	s_addc_u32 s1, s17, s21
	s_add_u32 s0, s0, 0xc000
	s_addc_u32 s1, s1, 0
	s_add_i32 s22, s31, s63
	s_add_u32 s2, s18, s20
	s_addc_u32 s3, s19, s21
	s_add_u32 s2, s2, 0xc000
	s_mov_b32 s24, m0
	s_mov_b32 m0, s22
	s_nop 0
	global_load_lds_dwordx4 v172, s[0:1]
	s_mov_b32 m0, s24
	s_addc_u32 s3, s3, 0
	s_add_i32 s23, s31, s64
	s_mov_b32 s0, m0
	s_mov_b32 m0, s23
	s_nop 0
	global_load_lds_dwordx4 v173, s[2:3]
	s_mov_b32 m0, s0
	global_load_dwordx2 v[148:149], v[146:147], off sc1
